# cmp-attn stats pass: exp-sum chain restructured (in-place fmamk, batched exp, same-order adds, no trans nops)
# speedup vs baseline: 1.0025x; 1.0025x over previous
;     ...
;                         } else if (MODE == 2) {
;                             const float mn = fmaxf(mrun[qd], mx), corr = __expf(mrun[qd] - mn); mrun[qd] = mn; float ps = 0.f;
;                             const float negm0 = (mn < -1e29f ? 0.f : -mn * L2E) + boff;
; #pragma unroll
;                             for (int kt = 0; kt < 4; ++kt)
; #pragma unroll
;                                 for (int r = 0; r < 4; ++r) ps += __builtin_amdgcn_exp2f(__builtin_fmaf(sc[kt][r], L2E, negm0));
;                             lrun[qd] = lrun[qd] * corr + ps;
.LBB0_890:
	v_max3_f32 v167, v134, v135, v136
	v_max3_f32 v167, v167, v137, v130
	v_max3_f32 v167, v167, v131, v132
	v_max3_f32 v167, v167, v133, v126
	v_max3_f32 v167, v167, v127, v128
	v_max3_f32 v167, v167, v129, v122
	v_max3_f32 v167, v167, v123, v124
	v_max_f32_e32 v167, v167, v125
	v_add_f32_e32 v166, v166, v167
	v_max_f32_e32 v167, v164, v164
	v_max_f32_e32 v166, v167, v166
	v_sub_f32_e32 v167, v164, v166
	v_mul_f32_e32 v167, 0x3fb8aa3b, v167
	v_exp_f32_e32 v192, v167
	v_mul_f32_e32 v167, 0xbfb8aa3b, v166
	v_cmp_ngt_f32_e32 vcc, s30, v166
	s_nop 1
	v_cndmask_b32_e32 v167, 0, v167, vcc
	v_add_f32_e32 v167, v191, v167
	v_fmamk_f32 v134, v134, 0x3fb8aa3b, v167
	v_fmamk_f32 v135, v135, 0x3fb8aa3b, v167
	v_fmamk_f32 v136, v136, 0x3fb8aa3b, v167
	v_fmamk_f32 v137, v137, 0x3fb8aa3b, v167
	v_fmamk_f32 v130, v130, 0x3fb8aa3b, v167
	v_fmamk_f32 v131, v131, 0x3fb8aa3b, v167
	v_fmamk_f32 v132, v132, 0x3fb8aa3b, v167
	v_fmamk_f32 v133, v133, 0x3fb8aa3b, v167
	v_fmamk_f32 v126, v126, 0x3fb8aa3b, v167
	v_fmamk_f32 v127, v127, 0x3fb8aa3b, v167
	v_fmamk_f32 v128, v128, 0x3fb8aa3b, v167
	v_fmamk_f32 v129, v129, 0x3fb8aa3b, v167
	v_fmamk_f32 v122, v122, 0x3fb8aa3b, v167
	v_fmamk_f32 v123, v123, 0x3fb8aa3b, v167
	v_fmamk_f32 v124, v124, 0x3fb8aa3b, v167
	v_fmac_f32_e32 v167, 0x3fb8aa3b, v125
	v_exp_f32_e32 v134, v134
	v_exp_f32_e32 v135, v135
	v_exp_f32_e32 v136, v136
	v_exp_f32_e32 v137, v137
	v_exp_f32_e32 v130, v130
	v_exp_f32_e32 v131, v131
	v_exp_f32_e32 v132, v132
	v_exp_f32_e32 v133, v133
	v_exp_f32_e32 v126, v126
	v_exp_f32_e32 v127, v127
	v_exp_f32_e32 v128, v128
	v_exp_f32_e32 v129, v129
	v_exp_f32_e32 v122, v122
	v_exp_f32_e32 v123, v123
	v_exp_f32_e32 v124, v124
	v_exp_f32_e32 v167, v167
	v_add_f32_e32 v193, v135, v134
	v_add_f32_e32 v193, v136, v193
	v_add_f32_e32 v193, v137, v193
	v_add_f32_e32 v193, v130, v193
	v_add_f32_e32 v193, v131, v193
	v_add_f32_e32 v193, v132, v193
	v_add_f32_e32 v193, v133, v193
	v_add_f32_e32 v193, v126, v193
	v_add_f32_e32 v193, v127, v193
	v_add_f32_e32 v193, v128, v193
	v_add_f32_e32 v193, v129, v193
	v_add_f32_e32 v193, v122, v193
	v_add_f32_e32 v193, v123, v193
	v_add_f32_e32 v193, v124, v193
	v_add_f32_e32 v193, v167, v193
	v_fmac_f32_e32 v193, v162, v192
	v_mov_b32_e32 v167, v165
	v_mov_b32_e32 v162, v193
	s_cbranch_execnz .LBB0_892

;     ...
;                         { float m = fmaxf(fmaxf(sc[0][0], sc[0][1]), sc[0][2]);
;                           m = fmaxf(fmaxf(m, sc[0][3]), sc[1][0]); m = fmaxf(fmaxf(m, sc[1][1]), sc[1][2]); m = fmaxf(fmaxf(m, sc[1][3]), sc[2][0]);
;                           m = fmaxf(fmaxf(m, sc[2][1]), sc[2][2]); m = fmaxf(fmaxf(m, sc[2][3]), sc[3][0]); m = fmaxf(fmaxf(m, sc[3][1]), sc[3][2]); mx = fmaxf(m, sc[3][3]) + bshift; }
;                         if (MODE == 3 && !colsel) mx = -1e30f;
;                         float p[4][4];
;                         constexpr float L2E = 1.4426950408889634f;
;                         if (MODE == 2 && pass == 1) {
;                             const float negm1 = (mrun[qd] < -1e29f ? 0.f : -mrun[qd] * L2E) + boff + linv[qd];
; #pragma unroll
;                             for (int kt = 0; kt < 4; ++kt)
; #pragma unroll
;                                 for (int r = 0; r < 4; ++r) p[kt][r] = __builtin_amdgcn_exp2f(__builtin_fmaf(sc[kt][r], L2E, negm1));
;                         } else if (MODE == 2) {
;                             const float mn = fmaxf(mrun[qd], mx), corr = __expf(mrun[qd] - mn); mrun[qd] = mn; float ps = 0.f;
;                             const float negm0 = (mn < -1e29f ? 0.f : -mn * L2E) + boff;
; #pragma unroll
;                             for (int kt = 0; kt < 4; ++kt)
; #pragma unroll
;                                 for (int r = 0; r < 4; ++r) ps += __builtin_amdgcn_exp2f(__builtin_fmaf(sc[kt][r], L2E, negm0));
;                             lrun[qd] = lrun[qd] * corr + ps;
.LBB0_906:
	v_max3_f32 v104, v114, v115, v116
	v_max3_f32 v104, v104, v117, v98
	v_max3_f32 v104, v104, v99, v100
	v_max3_f32 v104, v104, v101, v94
	v_max3_f32 v104, v104, v95, v96
	v_max3_f32 v104, v104, v97, v90
	v_max3_f32 v104, v104, v91, v92
	v_max_f32_e32 v104, v104, v93
	v_add_f32_e32 v103, v103, v104
	v_max_f32_e32 v104, v167, v167
	v_max_f32_e32 v165, v104, v103
	v_mul_f32_e32 v104, 0xbfb8aa3b, v165
	v_cmp_ngt_f32_e32 vcc, s30, v165
	v_sub_f32_e32 v103, v167, v165
	v_mul_f32_e32 v103, 0x3fb8aa3b, v103
	v_cndmask_b32_e32 v104, 0, v104, vcc
	v_add_f32_e32 v104, v102, v104
	v_exp_f32_e32 v103, v103
	v_mov_b32_e32 v164, v166
	v_fmamk_f32 v114, v114, 0x3fb8aa3b, v104
	v_fmamk_f32 v115, v115, 0x3fb8aa3b, v104
	v_fmamk_f32 v116, v116, 0x3fb8aa3b, v104
	v_fmamk_f32 v117, v117, 0x3fb8aa3b, v104
	v_fmamk_f32 v98, v98, 0x3fb8aa3b, v104
	v_fmamk_f32 v99, v99, 0x3fb8aa3b, v104
	v_fmamk_f32 v100, v100, 0x3fb8aa3b, v104
	v_fmamk_f32 v101, v101, 0x3fb8aa3b, v104
	v_fmamk_f32 v94, v94, 0x3fb8aa3b, v104
	v_fmamk_f32 v95, v95, 0x3fb8aa3b, v104
	v_fmamk_f32 v96, v96, 0x3fb8aa3b, v104
	v_fmamk_f32 v97, v97, 0x3fb8aa3b, v104
	v_fmamk_f32 v90, v90, 0x3fb8aa3b, v104
	v_fmamk_f32 v91, v91, 0x3fb8aa3b, v104
	v_fmamk_f32 v92, v92, 0x3fb8aa3b, v104
	v_fmac_f32_e32 v104, 0x3fb8aa3b, v93
	v_exp_f32_e32 v114, v114
	v_exp_f32_e32 v115, v115
	v_exp_f32_e32 v116, v116
	v_exp_f32_e32 v117, v117
	v_exp_f32_e32 v98, v98
	v_exp_f32_e32 v99, v99
	v_exp_f32_e32 v100, v100
	v_exp_f32_e32 v101, v101
	v_exp_f32_e32 v94, v94
	v_exp_f32_e32 v95, v95
	v_exp_f32_e32 v96, v96
	v_exp_f32_e32 v97, v97
	v_exp_f32_e32 v90, v90
	v_exp_f32_e32 v91, v91
	v_exp_f32_e32 v92, v92
	v_exp_f32_e32 v104, v104
	v_add_f32_e32 v105, v115, v114
	v_add_f32_e32 v105, v116, v105
	v_add_f32_e32 v105, v117, v105
	v_add_f32_e32 v105, v98, v105
	v_add_f32_e32 v105, v99, v105
	v_add_f32_e32 v105, v100, v105
	v_add_f32_e32 v105, v101, v105
	v_add_f32_e32 v105, v94, v105
	v_add_f32_e32 v105, v95, v105
	v_add_f32_e32 v105, v96, v105
	v_add_f32_e32 v105, v97, v105
	v_add_f32_e32 v105, v90, v105
	v_add_f32_e32 v105, v91, v105
	v_add_f32_e32 v105, v92, v105
	v_add_f32_e32 v104, v104, v105
	v_fmac_f32_e32 v104, v163, v103
	v_mov_b32_e32 v163, v104
	s_cbranch_execnz .LBB0_908
